# down-projection epilogue bias vectors also loaded at the unit top: no vmcnt wait in either expert-GEMM epilogue
# baseline (speedup 1.0000x reference)
;     __device__ __forceinline__ void operator()(const f32x4 (&acc)[2][2][4][2], const Unit& u, int wr, int wc, int fr, int fq) const {
;         const int row0 = u.pm * BM + wr * 64 + fr, col0 = u.pn * BM + wc * 32 + 8 * fq;
;         const float* b = bd + (size_t)u.e * D + col0;
;         f32x4 bv[2][2];
; #pragma unroll
;         for (int bj = 0; bj < 2; ++bj)
; #pragma unroll
;             for (int n = 0; n < 2; ++n) bv[bj][n] = *(const f32x4*)(b + bj * HALF + 4 * n) * oscale;
; template <class Epi, bool GATHER, int MODE, bool SPLIT = false>
; __device__ __forceinline__ void gemm_phase(PG8_LAS unsigned char* lds, const Gemm g, const Order& S, const Epi& E) {
;     ...
;         const bool has_next = S.next(ui + 1, nxt);
.LBB0_870:
	s_lshl_b32 s99, s20, 8
	v_ashrrev_i32_e32 v213, 31, v164
	v_mov_b32_e32 v212, v164
	v_or_b32_e32 v214, s99, v171
	v_lshlrev_b64 v[212:213], 13, v[212:213]
	v_lshl_add_u64 v[212:213], s[88:89], 0, v[212:213]
	v_ashrrev_i32_e32 v215, 31, v214
	v_lshl_add_u64 v[212:213], v[214:215], 2, v[212:213]
	global_load_dwordx4 v[216:219], v[212:213], off
	global_load_dwordx4 v[220:223], v[212:213], off offset:16
	global_load_dwordx4 v[224:227], v[212:213], off offset:512
	global_load_dwordx4 v[232:235], v[212:213], off offset:528
	s_add_i32 s40, s40, 1
	s_mul_i32 s1, s40, s55
	s_mul_hi_u32 s2, s40, s33
	s_add_i32 s2, s2, s1
	s_mul_i32 s1, s40, s33
	s_add_u32 s26, s1, s92
	s_addc_u32 s27, s2, s38
	v_cmp_lt_i64_e64 s[2:3], s[26:27], v[162:163]
	s_mov_b64 s[28:29], -1
	s_and_b64 vcc, exec, s[2:3]
	s_cbranch_vccnz .LBB0_872
	s_ashr_i32 s17, s16, 31
	s_mov_b64 s[28:29], 0

; __device__ __forceinline__ void swap16(int& x, int& y) { const auto r = __builtin_amdgcn_permlane16_swap((unsigned)x, (unsigned)y, false, false); x = (int)r[0]; y = (int)r[1]; }
;     __device__ __forceinline__ void operator()(const f32x4 (&acc)[2][2][4][2], const Unit& u, int wr, int wc, int fr, int fq) const {
;         const int row0 = u.pm * BM + wr * 64 + fr, col0 = u.pn * BM + wc * 32 + 8 * fq;
;         const float* b = bd + (size_t)u.e * D + col0;
;         f32x4 bv[2][2];
; #pragma unroll
;         for (int bj = 0; bj < 2; ++bj)
; #pragma unroll
;             for (int n = 0; n < 2; ++n) bv[bj][n] = *(const f32x4*)(b + bj * HALF + 4 * n) * oscale;
;         const float ds = descale * oscale;
;         const int colw = col0 & ~8, odd = fq & 1;
; #pragma unroll
;         for (int ai = 0; ai < 2; ++ai)
; #pragma unroll
;             for (int bj = 0; bj < 2; ++bj) {
;                 int w0[4], w1[4];
; #pragma unroll
;                 for (int m = 0; m < 4; ++m) {
;                     f32x4 o0 = acc[ai][bj][m][0] * ds + bv[bj][0], o1 = acc[ai][bj][m][1] * ds + bv[bj][1];
; #pragma unroll
;                     for (int j = 0; j < 4; ++j) { o0[j] = fminf(fmaxf(o0[j], -448.0f), 448.0f); o1[j] = fminf(fmaxf(o1[j], -448.0f), 448.0f); }
;                     w0[m] = __builtin_amdgcn_cvt_pk_fp8_f32(o0[0], o0[1], 0, false); w0[m] = __builtin_amdgcn_cvt_pk_fp8_f32(o0[2], o0[3], w0[m], true);
;                     w1[m] = __builtin_amdgcn_cvt_pk_fp8_f32(o1[0], o1[1], 0, false); w1[m] = __builtin_amdgcn_cvt_pk_fp8_f32(o1[2], o1[3], w1[m], true);
;                 }
; #pragma unroll
;                 for (int p = 0; p < 2; ++p) { swap16(w0[2 * p], w0[2 * p + 1]); swap16(w1[2 * p], w1[2 * p + 1]);
;                     u32x4 w; w.x = (unsigned)w0[2 * p]; w.y = (unsigned)w1[2 * p]; w.z = (unsigned)w0[2 * p + 1]; w.w = (unsigned)w1[2 * p + 1];
;                     *(u32x4*)(YS + (size_t)(row0 + ai * HALF + (2 * p + odd) * 16) * D + colw + bj * HALF) = w; }
.LBB0_878:
	s_lshl_b32 s1, s20, 8
	s_nop 15
	s_nop 15
	v_mov_b32_e32 v28, 0
	v_mov_b32_e32 v183, 0
	v_mov_b32_e32 v29, 0
	v_mov_b32_e32 v30, 0
	v_mov_b32_e32 v31, 0
	v_lshl_add_u32 v164, s0, 8, v168
	v_bitop3_b32 v10, s1, v177, v171 bitop3:0xc8
	v_ashrrev_i32_e32 v11, 31, v10
	v_mov_b32_e32 v180, 0
	v_mov_b32_e32 v181, 0
	v_mov_b32_e32 v182, 0
	s_andn2_b64 vcc, exec, s[2:3]
	s_mov_b64 s[0:1], -1
	v_pk_mul_f32 v[18:19], v[216:217], s[10:11] op_sel_hi:[1,0]
	v_pk_mul_f32 v[14:15], v[220:221], s[10:11] op_sel_hi:[1,0]
	v_pk_mul_f32 v[6:7], v[226:227], s[10:11] op_sel_hi:[1,0]
	v_pk_fma_f32 v[22:23], v[158:159], s[12:13], v[18:19] op_sel_hi:[1,0,1]
	v_pk_fma_f32 v[130:131], v[130:131], s[12:13], v[14:15] op_sel_hi:[1,0,1]
	v_med3_f32 v22, v22, s56, v178
	v_med3_f32 v23, v23, s56, v178
	v_med3_f32 v130, v130, s56, v178
	v_med3_f32 v131, v131, s56, v178
	v_cvt_pk_fp8_f32 v28, v22, v23
	v_pk_mul_f32 v[16:17], v[218:219], s[10:11] op_sel_hi:[1,0]
	v_cvt_pk_fp8_f32 v183, v130, v131
	v_pk_mul_f32 v[12:13], v[222:223], s[10:11] op_sel_hi:[1,0]
	v_pk_mul_f32 v[8:9], v[224:225], s[10:11] op_sel_hi:[1,0]
	v_pk_mul_f32 v[2:3], v[234:235], s[10:11] op_sel_hi:[1,0]
	v_pk_fma_f32 v[20:21], v[160:161], s[12:13], v[16:17] op_sel_hi:[1,0,1]
	v_pk_fma_f32 v[26:27], v[154:155], s[12:13], v[14:15] op_sel_hi:[1,0,1]
	v_pk_fma_f32 v[150:151], v[150:151], s[12:13], v[18:19] op_sel_hi:[1,0,1]
	v_pk_fma_f32 v[146:147], v[146:147], s[12:13], v[14:15] op_sel_hi:[1,0,1]
	v_pk_fma_f32 v[132:133], v[132:133], s[12:13], v[12:13] op_sel_hi:[1,0,1]
	v_med3_f32 v26, v26, s56, v178
	v_med3_f32 v27, v27, s56, v178
	v_med3_f32 v20, v20, s56, v178
	v_med3_f32 v21, v21, s56, v178
	v_med3_f32 v150, v150, s56, v178
	v_med3_f32 v146, v146, s56, v178
	v_med3_f32 v151, v151, s56, v178
	v_med3_f32 v147, v147, s56, v178
	v_med3_f32 v132, v132, s56, v178
	v_cvt_pk_fp8_f32 v29, v26, v27
	v_cvt_pk_fp8_f32 v30, v150, v151
	v_cvt_pk_fp8_f32 v31, v146, v147
	v_cvt_pk_fp8_f32 v28, v20, v21 op_sel:[0,0,1]
	v_med3_f32 v20, v133, s56, v178
	v_cvt_pk_fp8_f32 v183, v132, v20 op_sel:[0,0,1]
	v_or_b32_e32 v20, v164, v169
	v_pk_mul_f32 v[4:5], v[232:233], s[10:11] op_sel_hi:[1,0]
	v_pk_fma_f32 v[24:25], v[156:157], s[12:13], v[12:13] op_sel_hi:[1,0,1]
	v_pk_fma_f32 v[32:33], v[152:153], s[12:13], v[16:17] op_sel_hi:[1,0,1]
	v_pk_fma_f32 v[148:149], v[148:149], s[12:13], v[12:13] op_sel_hi:[1,0,1]
	v_ashrrev_i32_e32 v21, 31, v20
	v_med3_f32 v24, v24, s56, v178
	v_med3_f32 v25, v25, s56, v178
	v_med3_f32 v32, v32, s56, v178
	v_med3_f32 v148, v148, s56, v178
	v_med3_f32 v33, v33, s56, v178
	v_med3_f32 v149, v149, s56, v178
	v_lshlrev_b64 v[20:21], 11, v[20:21]
	v_cvt_pk_fp8_f32 v29, v24, v25 op_sel:[0,0,1]
	v_cvt_pk_fp8_f32 v30, v32, v33 op_sel:[0,0,1]
	v_cvt_pk_fp8_f32 v31, v148, v149 op_sel:[0,0,1]
	v_lshl_add_u64 v[20:21], s[6:7], 0, v[20:21]
	v_lshl_add_u64 v[32:33], v[20:21], 0, v[10:11]
	v_or_b32_e32 v20, v164, v170
	v_ashrrev_i32_e32 v21, 31, v20
	v_lshlrev_b64 v[20:21], 11, v[20:21]
	v_permlane16_swap_b32_e32 v28, v30
	v_permlane16_swap_b32_e32 v29, v31
	v_lshl_add_u64 v[20:21], s[6:7], 0, v[20:21]
	global_store_dwordx4 v[32:33], v[28:31], off
	v_pk_fma_f32 v[22:23], v[128:129], s[12:13], v[6:7] op_sel_hi:[1,0,1]
	v_pk_fma_f32 v[26:27], v[122:123], s[12:13], v[4:5] op_sel_hi:[1,0,1]
	v_lshl_add_u64 v[28:29], v[20:21], 0, v[10:11]
	v_pk_fma_f32 v[20:21], v[126:127], s[12:13], v[8:9] op_sel_hi:[1,0,1]
	v_med3_f32 v26, v26, s56, v178
	v_med3_f32 v30, v20, s56, v178
	v_med3_f32 v21, v21, s56, v178
	v_mov_b32_e32 v20, 0
	v_cvt_pk_fp8_f32 v20, v30, v21
	v_med3_f32 v27, v27, s56, v178
	v_med3_f32 v22, v22, s56, v178
	v_mov_b32_e32 v21, 0
	v_med3_f32 v23, v23, s56, v178
	v_cvt_pk_fp8_f32 v21, v26, v27
	v_cvt_pk_fp8_f32 v20, v22, v23 op_sel:[0,0,1]
	v_pk_fma_f32 v[22:23], v[118:119], s[12:13], v[8:9] op_sel_hi:[1,0,1]
	v_pk_fma_f32 v[30:31], v[114:115], s[12:13], v[4:5] op_sel_hi:[1,0,1]
	v_med3_f32 v114, v22, s56, v178
	v_med3_f32 v23, v23, s56, v178
	v_mov_b32_e32 v22, 0
	v_pk_fma_f32 v[24:25], v[124:125], s[12:13], v[2:3] op_sel_hi:[1,0,1]
	v_cvt_pk_fp8_f32 v22, v114, v23
	v_med3_f32 v24, v24, s56, v178
	v_med3_f32 v25, v25, s56, v178
	v_cvt_pk_fp8_f32 v21, v24, v25 op_sel:[0,0,1]
	v_pk_fma_f32 v[24:25], v[120:121], s[12:13], v[6:7] op_sel_hi:[1,0,1]
	v_med3_f32 v30, v30, s56, v178
	v_med3_f32 v31, v31, s56, v178
	v_med3_f32 v24, v24, s56, v178
	v_mov_b32_e32 v23, 0
	v_med3_f32 v25, v25, s56, v178
	v_cvt_pk_fp8_f32 v23, v30, v31
	v_cvt_pk_fp8_f32 v22, v24, v25 op_sel:[0,0,1]
	v_pk_fma_f32 v[24:25], v[110:111], s[12:13], v[8:9] op_sel_hi:[1,0,1]
	v_pk_fma_f32 v[30:31], v[108:109], s[12:13], v[2:3] op_sel_hi:[1,0,1]
	v_med3_f32 v108, v24, s56, v178
	v_med3_f32 v25, v25, s56, v178
	v_mov_b32_e32 v24, 0
	v_pk_fma_f32 v[26:27], v[116:117], s[12:13], v[2:3] op_sel_hi:[1,0,1]
	v_cvt_pk_fp8_f32 v24, v108, v25
	v_med3_f32 v26, v26, s56, v178
	v_med3_f32 v27, v27, s56, v178
	v_cvt_pk_fp8_f32 v23, v26, v27 op_sel:[0,0,1]
	v_pk_fma_f32 v[26:27], v[112:113], s[12:13], v[6:7] op_sel_hi:[1,0,1]
	v_pk_fma_f32 v[106:107], v[106:107], s[12:13], v[4:5] op_sel_hi:[1,0,1]
	v_med3_f32 v26, v26, s56, v178
	v_med3_f32 v27, v27, s56, v178
	v_med3_f32 v106, v106, s56, v178
	v_med3_f32 v107, v107, s56, v178
	v_mov_b32_e32 v25, 0
	v_cvt_pk_fp8_f32 v24, v26, v27 op_sel:[0,0,1]
	v_pk_fma_f32 v[26:27], v[102:103], s[12:13], v[8:9] op_sel_hi:[1,0,1]
	v_pk_fma_f32 v[142:143], v[142:143], s[12:13], v[18:19] op_sel_hi:[1,0,1]
	v_pk_fma_f32 v[138:139], v[138:139], s[12:13], v[14:15] op_sel_hi:[1,0,1]
	v_pk_fma_f32 v[134:135], v[134:135], s[12:13], v[18:19] op_sel_hi:[1,0,1]
	v_cvt_pk_fp8_f32 v25, v106, v107
; __device__ __forceinline__ void swap16(int& x, int& y) { const auto r = __builtin_amdgcn_permlane16_swap((unsigned)x, (unsigned)y, false, false); x = (int)r[0]; y = (int)r[1]; }
;     __device__ __forceinline__ void operator()(const f32x4 (&acc)[2][2][4][2], const Unit& u, int wr, int wc, int fr, int fq) const {
;     ...
;             for (int bj = 0; bj < 2; ++bj) {
;                 int w0[4], w1[4];
; #pragma unroll
;                 for (int m = 0; m < 4; ++m) {
;                     f32x4 o0 = acc[ai][bj][m][0] * ds + bv[bj][0], o1 = acc[ai][bj][m][1] * ds + bv[bj][1];
; #pragma unroll
;                     for (int j = 0; j < 4; ++j) { o0[j] = fminf(fmaxf(o0[j], -448.0f), 448.0f); o1[j] = fminf(fmaxf(o1[j], -448.0f), 448.0f); }
;                     w0[m] = __builtin_amdgcn_cvt_pk_fp8_f32(o0[0], o0[1], 0, false); w0[m] = __builtin_amdgcn_cvt_pk_fp8_f32(o0[2], o0[3], w0[m], true);
;                     w1[m] = __builtin_amdgcn_cvt_pk_fp8_f32(o1[0], o1[1], 0, false); w1[m] = __builtin_amdgcn_cvt_pk_fp8_f32(o1[2], o1[3], w1[m], true);
;                 }
; #pragma unroll
;                 for (int p = 0; p < 2; ++p) { swap16(w0[2 * p], w0[2 * p + 1]); swap16(w1[2 * p], w1[2 * p + 1]);
;                     u32x4 w; w.x = (unsigned)w0[2 * p]; w.y = (unsigned)w1[2 * p]; w.z = (unsigned)w0[2 * p + 1]; w.w = (unsigned)w1[2 * p + 1];
;                     *(u32x4*)(YS + (size_t)(row0 + ai * HALF + (2 * p + odd) * 16) * D + colw + bj * HALF) = w; }
	v_pk_fma_f32 v[98:99], v[98:99], s[12:13], v[4:5] op_sel_hi:[1,0,1]
	v_med3_f32 v102, v26, s56, v178
	v_med3_f32 v27, v27, s56, v178
	v_mov_b32_e32 v26, 0
	v_med3_f32 v142, v142, s56, v178
	v_med3_f32 v138, v138, s56, v178
	v_med3_f32 v143, v143, s56, v178
	v_med3_f32 v139, v139, s56, v178
	v_med3_f32 v134, v134, s56, v178
	v_med3_f32 v135, v135, s56, v178
	v_med3_f32 v98, v98, s56, v178
	v_med3_f32 v99, v99, s56, v178
	v_cvt_pk_fp8_f32 v26, v102, v27
	v_mov_b32_e32 v27, 0
	v_cvt_pk_fp8_f32 v180, v142, v143
	v_cvt_pk_fp8_f32 v181, v138, v139
	v_cvt_pk_fp8_f32 v182, v134, v135
	v_cvt_pk_fp8_f32 v27, v98, v99
	v_med3_f32 v30, v30, s56, v178
	v_med3_f32 v31, v31, s56, v178
	v_pk_fma_f32 v[144:145], v[144:145], s[12:13], v[16:17] op_sel_hi:[1,0,1]
	v_pk_fma_f32 v[140:141], v[140:141], s[12:13], v[12:13] op_sel_hi:[1,0,1]
	v_pk_fma_f32 v[136:137], v[136:137], s[12:13], v[16:17] op_sel_hi:[1,0,1]
	v_cvt_pk_fp8_f32 v25, v30, v31 op_sel:[0,0,1]
	v_pk_fma_f32 v[30:31], v[104:105], s[12:13], v[6:7] op_sel_hi:[1,0,1]
	v_pk_fma_f32 v[100:101], v[100:101], s[12:13], v[2:3] op_sel_hi:[1,0,1]
	v_med3_f32 v144, v144, s56, v178
	v_med3_f32 v140, v140, s56, v178
	v_med3_f32 v145, v145, s56, v178
	v_med3_f32 v141, v141, s56, v178
	v_med3_f32 v136, v136, s56, v178
	v_med3_f32 v137, v137, s56, v178
	v_med3_f32 v30, v30, s56, v178
	v_med3_f32 v100, v100, s56, v178
	v_med3_f32 v31, v31, s56, v178
	v_med3_f32 v98, v101, s56, v178
	v_cvt_pk_fp8_f32 v180, v144, v145 op_sel:[0,0,1]
	v_cvt_pk_fp8_f32 v181, v140, v141 op_sel:[0,0,1]
	v_cvt_pk_fp8_f32 v182, v136, v137 op_sel:[0,0,1]
	v_cvt_pk_fp8_f32 v26, v30, v31 op_sel:[0,0,1]
	v_cvt_pk_fp8_f32 v27, v100, v98 op_sel:[0,0,1]
	v_permlane16_swap_b32_e32 v20, v22
	v_permlane16_swap_b32_e32 v21, v23
	v_permlane16_swap_b32_e32 v180, v182
	v_permlane16_swap_b32_e32 v181, v183
	global_store_dwordx4 v[32:33], v[20:23], off offset:128
	v_permlane16_swap_b32_e32 v24, v26
	v_permlane16_swap_b32_e32 v25, v27
	v_pk_fma_f32 v[20:21], v[94:95], s[12:13], v[18:19] op_sel_hi:[1,0,1]
	global_store_dwordx4 v[28:29], v[180:183], off
	global_store_dwordx4 v[28:29], v[24:27], off offset:128
	v_med3_f32 v28, v20, s56, v178
	v_med3_f32 v21, v21, s56, v178
	v_mov_b32_e32 v20, 0
	v_cvt_pk_fp8_f32 v20, v28, v21
	v_pk_fma_f32 v[22:23], v[96:97], s[12:13], v[16:17] op_sel_hi:[1,0,1]
	v_pk_fma_f32 v[26:27], v[90:91], s[12:13], v[14:15] op_sel_hi:[1,0,1]
	v_med3_f32 v22, v22, s56, v178
	v_med3_f32 v26, v26, s56, v178
	v_med3_f32 v27, v27, s56, v178
	v_mov_b32_e32 v21, 0
	v_med3_f32 v23, v23, s56, v178
	v_cvt_pk_fp8_f32 v21, v26, v27
	v_cvt_pk_fp8_f32 v20, v22, v23 op_sel:[0,0,1]
	v_pk_fma_f32 v[22:23], v[86:87], s[12:13], v[18:19] op_sel_hi:[1,0,1]
	v_pk_fma_f32 v[24:25], v[92:93], s[12:13], v[12:13] op_sel_hi:[1,0,1]
	v_med3_f32 v30, v22, s56, v178
	v_med3_f32 v23, v23, s56, v178
	v_mov_b32_e32 v22, 0
	v_cvt_pk_fp8_f32 v22, v30, v23
	v_med3_f32 v24, v24, s56, v178
	v_med3_f32 v25, v25, s56, v178
	v_cvt_pk_fp8_f32 v21, v24, v25 op_sel:[0,0,1]
	v_pk_fma_f32 v[24:25], v[88:89], s[12:13], v[16:17] op_sel_hi:[1,0,1]
	v_pk_fma_f32 v[28:29], v[82:83], s[12:13], v[14:15] op_sel_hi:[1,0,1]
	v_med3_f32 v24, v24, s56, v178
	v_med3_f32 v28, v28, s56, v178
	v_med3_f32 v29, v29, s56, v178
	v_mov_b32_e32 v23, 0
	v_med3_f32 v25, v25, s56, v178
	v_cvt_pk_fp8_f32 v23, v28, v29
	v_cvt_pk_fp8_f32 v22, v24, v25 op_sel:[0,0,1]
	v_pk_fma_f32 v[24:25], v[78:79], s[12:13], v[18:19] op_sel_hi:[1,0,1]
	v_pk_fma_f32 v[26:27], v[84:85], s[12:13], v[12:13] op_sel_hi:[1,0,1]
	v_med3_f32 v33, v24, s56, v178
	v_med3_f32 v25, v25, s56, v178
	v_mov_b32_e32 v24, 0
	v_cvt_pk_fp8_f32 v24, v33, v25
	v_med3_f32 v26, v26, s56, v178
	v_med3_f32 v27, v27, s56, v178
	v_cvt_pk_fp8_f32 v23, v26, v27 op_sel:[0,0,1]
	v_pk_fma_f32 v[26:27], v[80:81], s[12:13], v[16:17] op_sel_hi:[1,0,1]
	v_pk_fma_f32 v[30:31], v[74:75], s[12:13], v[14:15] op_sel_hi:[1,0,1]
	v_med3_f32 v26, v26, s56, v178
	v_med3_f32 v27, v27, s56, v178
	v_pk_fma_f32 v[14:15], v[66:67], s[12:13], v[14:15] op_sel_hi:[1,0,1]
	v_cvt_pk_fp8_f32 v24, v26, v27 op_sel:[0,0,1]
	v_med3_f32 v14, v14, s56, v178
	v_med3_f32 v15, v15, s56, v178
	v_mov_b32_e32 v27, 0
	v_cvt_pk_fp8_f32 v27, v14, v15
	v_pk_fma_f32 v[28:29], v[76:77], s[12:13], v[12:13] op_sel_hi:[1,0,1]
	v_pk_fma_f32 v[12:13], v[68:69], s[12:13], v[12:13] op_sel_hi:[1,0,1]
	v_add_u32_e32 v32, 0x80, v164
	v_med3_f32 v12, v12, s56, v178
	v_med3_f32 v13, v13, s56, v178
	v_cvt_pk_fp8_f32 v27, v12, v13 op_sel:[0,0,1]
	v_or_b32_e32 v12, v32, v169
; __device__ __forceinline__ void swap16(int& x, int& y) { const auto r = __builtin_amdgcn_permlane16_swap((unsigned)x, (unsigned)y, false, false); x = (int)r[0]; y = (int)r[1]; }
; #define PG8_BAR __builtin_amdgcn_s_barrier()
;     __device__ __forceinline__ void operator()(const f32x4 (&acc)[2][2][4][2], const Unit& u, int wr, int wc, int fr, int fq) const {
;     ...
;             for (int bj = 0; bj < 2; ++bj) {
;                 int w0[4], w1[4];
; #pragma unroll
;                 for (int m = 0; m < 4; ++m) {
;                     f32x4 o0 = acc[ai][bj][m][0] * ds + bv[bj][0], o1 = acc[ai][bj][m][1] * ds + bv[bj][1];
; #pragma unroll
;                     for (int j = 0; j < 4; ++j) { o0[j] = fminf(fmaxf(o0[j], -448.0f), 448.0f); o1[j] = fminf(fmaxf(o1[j], -448.0f), 448.0f); }
;                     w0[m] = __builtin_amdgcn_cvt_pk_fp8_f32(o0[0], o0[1], 0, false); w0[m] = __builtin_amdgcn_cvt_pk_fp8_f32(o0[2], o0[3], w0[m], true);
;                     w1[m] = __builtin_amdgcn_cvt_pk_fp8_f32(o1[0], o1[1], 0, false); w1[m] = __builtin_amdgcn_cvt_pk_fp8_f32(o1[2], o1[3], w1[m], true);
;                 }
; #pragma unroll
;                 for (int p = 0; p < 2; ++p) { swap16(w0[2 * p], w0[2 * p + 1]); swap16(w1[2 * p], w1[2 * p + 1]);
;                     u32x4 w; w.x = (unsigned)w0[2 * p]; w.y = (unsigned)w1[2 * p]; w.z = (unsigned)w0[2 * p + 1]; w.w = (unsigned)w1[2 * p + 1];
;                     *(u32x4*)(YS + (size_t)(row0 + ai * HALF + (2 * p + odd) * 16) * D + colw + bj * HALF) = w; }
; template <class Epi, bool GATHER, int MODE, bool SPLIT = false>
; __device__ __forceinline__ void gemm_phase(PG8_LAS unsigned char* lds, const Gemm g, const Order& S, const Epi& E) {
;     ...
;         if (!has_next) break;
; #pragma unroll
;         for (int a = 0; a < 2; ++a)
; #pragma unroll
;             for (int b = 0; b < 2; ++b)
; #pragma unroll
;                 for (int m = 0; m < 4; ++m)
; #pragma unroll
;                     for (int n = 0; n < 2; ++n) acc[a][b][m][n] = (f32x4){0.f, 0.f, 0.f, 0.f};
;         cur = nxt; cB = nB; cAr = nAr; ++ui;
; #pragma unroll
;         for (int h = 0; h < 2; ++h)
; #pragma unroll
;             for (int i = 0; i < 2; ++i) cv[h][i] = nv[h][i];
;         if (wr == 1) PG8_BAR;
	v_ashrrev_i32_e32 v13, 31, v12
	v_pk_fma_f32 v[18:19], v[70:71], s[12:13], v[18:19] op_sel_hi:[1,0,1]
	v_lshlrev_b64 v[12:13], 11, v[12:13]
	v_med3_f32 v18, v18, s56, v178
	v_med3_f32 v19, v19, s56, v178
	v_mov_b32_e32 v26, 0
	v_lshl_add_u64 v[12:13], s[6:7], 0, v[12:13]
	v_cvt_pk_fp8_f32 v26, v18, v19
	v_lshl_add_u64 v[18:19], v[12:13], 0, v[10:11]
	v_or_b32_e32 v12, v32, v170
	v_med3_f32 v30, v30, s56, v178
	v_med3_f32 v31, v31, s56, v178
	v_mov_b32_e32 v25, 0
	v_ashrrev_i32_e32 v13, 31, v12
	v_cvt_pk_fp8_f32 v25, v30, v31
	v_lshlrev_b64 v[12:13], 11, v[12:13]
	v_permlane16_swap_b32_e32 v20, v22
	v_permlane16_swap_b32_e32 v21, v23
	v_lshl_add_u64 v[12:13], s[6:7], 0, v[12:13]
	v_pk_fma_f32 v[16:17], v[72:73], s[12:13], v[16:17] op_sel_hi:[1,0,1]
	global_store_dwordx4 v[18:19], v[20:23], off
	v_med3_f32 v28, v28, s56, v178
	v_med3_f32 v29, v29, s56, v178
	v_lshl_add_u64 v[20:21], v[12:13], 0, v[10:11]
	v_pk_fma_f32 v[10:11], v[62:63], s[12:13], v[8:9] op_sel_hi:[1,0,1]
	v_med3_f32 v16, v16, s56, v178
	v_med3_f32 v14, v17, s56, v178
	v_med3_f32 v22, v10, s56, v178
	v_med3_f32 v11, v11, s56, v178
	v_mov_b32_e32 v10, 0
	v_cvt_pk_fp8_f32 v25, v28, v29 op_sel:[0,0,1]
	v_cvt_pk_fp8_f32 v26, v16, v14 op_sel:[0,0,1]
	v_cvt_pk_fp8_f32 v10, v22, v11
	v_pk_fma_f32 v[12:13], v[64:65], s[12:13], v[6:7] op_sel_hi:[1,0,1]
	v_pk_fma_f32 v[16:17], v[58:59], s[12:13], v[4:5] op_sel_hi:[1,0,1]
	v_med3_f32 v12, v12, s56, v178
	v_med3_f32 v16, v16, s56, v178
	v_med3_f32 v17, v17, s56, v178
	v_mov_b32_e32 v11, 0
	v_med3_f32 v13, v13, s56, v178
	v_permlane16_swap_b32_e32 v24, v26
	v_permlane16_swap_b32_e32 v25, v27
	v_cvt_pk_fp8_f32 v11, v16, v17
	v_cvt_pk_fp8_f32 v10, v12, v13 op_sel:[0,0,1]
	v_pk_fma_f32 v[12:13], v[54:55], s[12:13], v[8:9] op_sel_hi:[1,0,1]
	global_store_dwordx4 v[20:21], v[24:27], off
	v_med3_f32 v13, v13, s56, v178
	v_pk_fma_f32 v[14:15], v[60:61], s[12:13], v[2:3] op_sel_hi:[1,0,1]
	v_med3_f32 v24, v12, s56, v178
	v_mov_b32_e32 v12, 0
	v_cvt_pk_fp8_f32 v12, v24, v13
	v_med3_f32 v14, v14, s56, v178
	v_med3_f32 v15, v15, s56, v178
	v_cvt_pk_fp8_f32 v11, v14, v15 op_sel:[0,0,1]
	v_pk_fma_f32 v[14:15], v[56:57], s[12:13], v[6:7] op_sel_hi:[1,0,1]
	v_pk_fma_f32 v[22:23], v[50:51], s[12:13], v[4:5] op_sel_hi:[1,0,1]
	v_med3_f32 v14, v14, s56, v178
	v_med3_f32 v22, v22, s56, v178
	v_med3_f32 v23, v23, s56, v178
	v_mov_b32_e32 v13, 0
	v_med3_f32 v15, v15, s56, v178
	v_cvt_pk_fp8_f32 v13, v22, v23
	v_cvt_pk_fp8_f32 v12, v14, v15 op_sel:[0,0,1]
	v_pk_fma_f32 v[14:15], v[46:47], s[12:13], v[8:9] op_sel_hi:[1,0,1]
	v_pk_fma_f32 v[16:17], v[52:53], s[12:13], v[2:3] op_sel_hi:[1,0,1]
	v_med3_f32 v26, v14, s56, v178
	v_med3_f32 v15, v15, s56, v178
	v_mov_b32_e32 v14, 0
	v_cvt_pk_fp8_f32 v14, v26, v15
	v_med3_f32 v16, v16, s56, v178
	v_med3_f32 v17, v17, s56, v178
	v_cvt_pk_fp8_f32 v13, v16, v17 op_sel:[0,0,1]
	v_pk_fma_f32 v[16:17], v[48:49], s[12:13], v[6:7] op_sel_hi:[1,0,1]
	v_pk_fma_f32 v[24:25], v[42:43], s[12:13], v[4:5] op_sel_hi:[1,0,1]
	v_med3_f32 v16, v16, s56, v178
	v_med3_f32 v17, v17, s56, v178
	v_pk_fma_f32 v[8:9], v[38:39], s[12:13], v[8:9] op_sel_hi:[1,0,1]
	v_pk_fma_f32 v[4:5], v[34:35], s[12:13], v[4:5] op_sel_hi:[1,0,1]
	v_med3_f32 v24, v24, s56, v178
	v_med3_f32 v25, v25, s56, v178
	v_mov_b32_e32 v15, 0
	v_cvt_pk_fp8_f32 v14, v16, v17 op_sel:[0,0,1]
	v_med3_f32 v8, v8, s56, v178
	v_med3_f32 v4, v4, s56, v178
	v_med3_f32 v9, v9, s56, v178
	v_med3_f32 v5, v5, s56, v178
	v_mov_b32_e32 v16, 0
	v_mov_b32_e32 v17, 0
	v_cvt_pk_fp8_f32 v15, v24, v25
	v_cvt_pk_fp8_f32 v16, v8, v9
	v_cvt_pk_fp8_f32 v17, v4, v5
	v_pk_fma_f32 v[22:23], v[44:45], s[12:13], v[2:3] op_sel_hi:[1,0,1]
	v_pk_fma_f32 v[6:7], v[40:41], s[12:13], v[6:7] op_sel_hi:[1,0,1]
	v_pk_fma_f32 v[2:3], v[36:37], s[12:13], v[2:3] op_sel_hi:[1,0,1]
	v_med3_f32 v22, v22, s56, v178
	v_med3_f32 v23, v23, s56, v178
	v_med3_f32 v6, v6, s56, v178
	v_med3_f32 v2, v2, s56, v178
	v_med3_f32 v4, v7, s56, v178
	v_med3_f32 v3, v3, s56, v178
	v_cvt_pk_fp8_f32 v15, v22, v23 op_sel:[0,0,1]
	v_cvt_pk_fp8_f32 v16, v6, v4 op_sel:[0,0,1]
	v_cvt_pk_fp8_f32 v17, v2, v3 op_sel:[0,0,1]
	v_permlane16_swap_b32_e32 v10, v12
	v_permlane16_swap_b32_e32 v11, v13
	v_permlane16_swap_b32_e32 v14, v16
	v_permlane16_swap_b32_e32 v15, v17
	global_store_dwordx4 v[18:19], v[10:13], off offset:128
	global_store_dwordx4 v[20:21], v[14:17], off offset:128
	s_cbranch_vccnz .LBB0_869
	s_andn2_b64 vcc, exec, s[4:5]
	s_cbranch_vccnz .LBB0_868
	s_barrier
	s_branch .LBB0_868
